# v9: odd workgroups run the filters phase before the weight-conversion prologue (compute-bound and HBM-bound halves overlap)
# speedup vs baseline: 1.0186x; 1.0017x over previous
.LBB0_5:
	s_or_b64 exec, exec, s[2:3]
	s_lshr_b32 s70, s0, 6
	s_bitcmp1_b32 s88, 0
	s_cbranch_scc0 .Lpf_pro
	v_mov_b32_e32 v4, 0x27ffc
	v_mov_b32_e32 v0, 1
	ds_write_b32 v4, v0
	s_waitcnt lgkmcnt(0)
	s_branch .Lpf_filt
.Lpf_pro:
	s_mov_b64 s[10:11], s[96:97]
	s_mov_b32 s26, s70
	s_mov_b32 s0, -1
	s_mov_b32 s27, 0
	v_mbcnt_lo_u32_b32 v0, s0, 0
	v_mbcnt_hi_u32_b32 v0, s0, v0
	v_lshl_add_u32 v66, s26, 6, v0
	s_mov_b32 s0, s91
	s_mov_b32 s1, s88
	s_and_b32 s2, s0, 7
	s_cmp_lg_u32 s2, 0
	s_mov_b32 s24, 0
	s_cbranch_scc1 .LBB0_7
	s_ashr_i32 s3, s1, 31
	s_lshr_b32 s3, s3, 29
	s_add_i32 s3, s1, s3
	s_ashr_i32 s4, s3, 3
	s_and_b32 s3, s3, -8
	s_ashr_i32 s2, s0, 3
	s_sub_i32 s1, s1, s3
	s_mul_i32 s1, s1, s2
	s_add_i32 s1, s1, s4

.LBB0_123:
	v_mov_b32_e32 v4, 0x27ffc
	ds_read_b32 v5, v4
	s_waitcnt lgkmcnt(0)
	s_nop 0
	v_readfirstlane_b32 s0, v5
	s_nop 3
	s_cmp_eq_u32 s0, 2
	s_cbranch_scc1 .LBB0_252

.Lpf_chk:
	v_mov_b32_e32 v4, 0x27ffc
	ds_read_b32 v5, v4
	s_waitcnt lgkmcnt(0)
	s_nop 0
	v_readfirstlane_b32 s0, v5
	s_nop 3
	s_cmp_eq_u32 s0, 1
	s_cbranch_scc0 .LBB0_252
	s_barrier
	v_mov_b32_e32 v5, 2
	ds_write_b32 v4, v5
	s_waitcnt lgkmcnt(0)
	s_branch .Lpf_pro
